# route pass 3 rank loop: skip expert groups that were not selected (their masked scores are -inf and add 0), and issue the 8 lane-broadcasts of a group together with counted waits
# speedup vs baseline: 1.0371x; 1.0026x over previous
.LBB0_1886:
	s_lshr_b64 s[42:43], vcc, s40
	s_bitcmp1_b32 s42, 0
	s_cbranch_scc1 .Lrk_do_0
	v_add_u32_e32 v4, 32, v4
	s_add_i32 s40, s40, 8
	s_cmp_lg_u32 s40, 64
	s_cbranch_scc1 .LBB0_1886
	s_branch .Lrk_exit_0
.Lrk_do_0:
	v_subrev_u32_e32 v120, 28, v4
	ds_bpermute_b32 v112, v120, v3
	v_subrev_u32_e32 v121, 24, v4
	ds_bpermute_b32 v113, v121, v3
	v_subrev_u32_e32 v122, 20, v4
	ds_bpermute_b32 v114, v122, v3
	v_subrev_u32_e32 v123, 16, v4
	ds_bpermute_b32 v115, v123, v3
	v_subrev_u32_e32 v124, 12, v4
	ds_bpermute_b32 v116, v124, v3
	v_subrev_u32_e32 v125, 8, v4
	ds_bpermute_b32 v117, v125, v3
	v_subrev_u32_e32 v126, 4, v4
	ds_bpermute_b32 v118, v126, v3
	v_mov_b32_e32 v127, v4
	ds_bpermute_b32 v119, v127, v3
	v_add_u32_e32 v4, 32, v4
	v_cmp_lt_u32_e64 s[38:39], s40, v254
	s_waitcnt lgkmcnt(7)
	v_cmp_eq_f32_e64 s[36:37], v3, v112
	v_cmp_lt_f32_e64 s[34:35], v3, v112
	s_and_b64 s[36:37], s[38:39], s[36:37]
	s_or_b64 s[34:35], s[34:35], s[36:37]
	v_addc_co_u32_e64 v5, s[36:37], 0, v5, s[34:35]
	s_add_i32 s38, s40, 1
	v_cmp_lt_u32_e64 s[38:39], s38, v254
	s_waitcnt lgkmcnt(6)
	v_cmp_eq_f32_e64 s[36:37], v3, v113
	v_cmp_lt_f32_e64 s[34:35], v3, v113
	s_and_b64 s[36:37], s[38:39], s[36:37]
	s_or_b64 s[34:35], s[34:35], s[36:37]
	v_addc_co_u32_e64 v5, s[36:37], 0, v5, s[34:35]
	s_add_i32 s38, s40, 2
	v_cmp_lt_u32_e64 s[38:39], s38, v254
	s_waitcnt lgkmcnt(5)
	v_cmp_eq_f32_e64 s[36:37], v3, v114
	v_cmp_lt_f32_e64 s[34:35], v3, v114
	s_and_b64 s[36:37], s[38:39], s[36:37]
	s_or_b64 s[34:35], s[34:35], s[36:37]
	v_addc_co_u32_e64 v5, s[36:37], 0, v5, s[34:35]
	s_add_i32 s38, s40, 3
	v_cmp_lt_u32_e64 s[38:39], s38, v254
	s_waitcnt lgkmcnt(4)
	v_cmp_eq_f32_e64 s[36:37], v3, v115
	v_cmp_lt_f32_e64 s[34:35], v3, v115
	s_and_b64 s[36:37], s[38:39], s[36:37]
	s_or_b64 s[34:35], s[34:35], s[36:37]
	v_addc_co_u32_e64 v5, s[36:37], 0, v5, s[34:35]
	s_add_i32 s38, s40, 4
	v_cmp_lt_u32_e64 s[38:39], s38, v254
	s_waitcnt lgkmcnt(3)
	v_cmp_eq_f32_e64 s[36:37], v3, v116
	v_cmp_lt_f32_e64 s[34:35], v3, v116
	s_and_b64 s[36:37], s[38:39], s[36:37]
	s_or_b64 s[34:35], s[34:35], s[36:37]
	v_addc_co_u32_e64 v5, s[36:37], 0, v5, s[34:35]
	s_add_i32 s38, s40, 5
	v_cmp_lt_u32_e64 s[38:39], s38, v254
	s_waitcnt lgkmcnt(2)
	v_cmp_eq_f32_e64 s[36:37], v3, v117
	v_cmp_lt_f32_e64 s[34:35], v3, v117
	s_and_b64 s[36:37], s[38:39], s[36:37]
	s_or_b64 s[34:35], s[34:35], s[36:37]
	v_addc_co_u32_e64 v5, s[36:37], 0, v5, s[34:35]
	s_add_i32 s38, s40, 6
	v_cmp_lt_u32_e64 s[38:39], s38, v254
	s_waitcnt lgkmcnt(1)
	v_cmp_eq_f32_e64 s[36:37], v3, v118
	v_cmp_lt_f32_e64 s[34:35], v3, v118
	s_and_b64 s[36:37], s[38:39], s[36:37]
	s_or_b64 s[34:35], s[34:35], s[36:37]
	v_addc_co_u32_e64 v5, s[36:37], 0, v5, s[34:35]
	s_add_i32 s38, s40, 7
	v_cmp_lt_u32_e64 s[38:39], s38, v254
	s_waitcnt lgkmcnt(0)
	v_cmp_eq_f32_e64 s[36:37], v3, v119
	v_cmp_lt_f32_e64 s[34:35], v3, v119
	s_and_b64 s[36:37], s[38:39], s[36:37]
	s_or_b64 s[34:35], s[34:35], s[36:37]
	v_addc_co_u32_e64 v5, s[36:37], 0, v5, s[34:35]
	s_add_i32 s40, s40, 8
	s_cmp_lg_u32 s40, 64
	s_cbranch_scc1 .LBB0_1886
.Lrk_exit_0:
	v_cmp_gt_u32_e64 s[34:35], 8, v5
	s_and_b64 vcc, vcc, s[34:35]
	v_cndmask_b32_e32 v1, 0, v2, vcc
	ds_bpermute_b32 v3, v76, v1
	s_lshl_b32 s34, s64, 10
	s_add_i32 s40, s34, 0
	s_add_i32 s40, s40, 0x10600
	s_waitcnt lgkmcnt(0)
	v_add_f32_e32 v1, v1, v3
	ds_bpermute_b32 v3, v77, v1
	s_waitcnt lgkmcnt(0)
	v_add_f32_e32 v1, v1, v3
	ds_bpermute_b32 v3, v78, v1
	s_waitcnt lgkmcnt(0)
	v_add_f32_e32 v1, v1, v3
	ds_bpermute_b32 v3, v79, v1
	s_waitcnt lgkmcnt(0)
	v_add_f32_e32 v1, v1, v3
	ds_bpermute_b32 v3, v80, v1
	s_waitcnt lgkmcnt(0)
	v_add_f32_e32 v3, v1, v3
	ds_bpermute_b32 v4, v81, v3
	s_and_saveexec_b64 s[34:35], vcc
	s_cbranch_execz .LBB0_1889
	s_waitcnt lgkmcnt(0)
	v_add_f32_e32 v1, v3, v4
	v_div_scale_f32 v3, s[36:37], v1, v1, v2
	v_lshl_or_b32 v6, s60, 3, v5
	v_rcp_f32_e32 v10, v3
	v_ashrrev_i32_e32 v7, 31, v6
	v_lshlrev_b64 v[6:7], 2, v[6:7]
	v_lshl_add_u64 v[8:9], s[56:57], 0, v[6:7]
	ds_add_rtn_u32 v4, v85, v107
	global_store_dword v[8:9], v254, off
	v_fma_f32 v8, -v3, v10, 1.0
	v_fmac_f32_e32 v10, v8, v10
	v_div_scale_f32 v8, vcc, v2, v1, v2
	v_mul_f32_e32 v9, v8, v10
	v_fma_f32 v11, -v3, v9, v8
	v_fmac_f32_e32 v9, v11, v10
	v_fma_f32 v3, -v3, v9, v8
	v_div_fmas_f32 v3, v3, v10, v9
	v_div_fixup_f32 v1, v3, v1, v2
	v_mul_f32_e32 v1, 0x40200000, v1
	v_lshl_add_u64 v[2:3], s[58:59], 0, v[6:7]
	s_add_i32 s36, s40, s67
	global_store_dword v[2:3], v1, off
	s_waitcnt lgkmcnt(0)
	v_or_b32_e32 v1, v4, v86
	v_lshl_add_u32 v2, v5, 2, s36
	ds_write_b32 v2, v1

.LBB0_1890:
	s_lshr_b64 s[42:43], vcc, s41
	s_bitcmp1_b32 s42, 0
	s_cbranch_scc1 .Lrk_do_1
	v_add_u32_e32 v4, 32, v4
	s_add_i32 s41, s41, 8
	s_cmp_lg_u32 s41, 64
	s_cbranch_scc1 .LBB0_1890
	s_branch .Lrk_exit_1
.Lrk_do_1:
	v_subrev_u32_e32 v120, 28, v4
	ds_bpermute_b32 v112, v120, v3
	v_subrev_u32_e32 v121, 24, v4
	ds_bpermute_b32 v113, v121, v3
	v_subrev_u32_e32 v122, 20, v4
	ds_bpermute_b32 v114, v122, v3
	v_subrev_u32_e32 v123, 16, v4
	ds_bpermute_b32 v115, v123, v3
	v_subrev_u32_e32 v124, 12, v4
	ds_bpermute_b32 v116, v124, v3
	v_subrev_u32_e32 v125, 8, v4
	ds_bpermute_b32 v117, v125, v3
	v_subrev_u32_e32 v126, 4, v4
	ds_bpermute_b32 v118, v126, v3
	v_mov_b32_e32 v127, v4
	ds_bpermute_b32 v119, v127, v3
	v_add_u32_e32 v4, 32, v4
	v_cmp_lt_u32_e64 s[38:39], s41, v254
	s_waitcnt lgkmcnt(7)
	v_cmp_eq_f32_e64 s[36:37], v3, v112
	v_cmp_lt_f32_e64 s[34:35], v3, v112
	s_and_b64 s[36:37], s[38:39], s[36:37]
	s_or_b64 s[34:35], s[34:35], s[36:37]
	v_addc_co_u32_e64 v5, s[36:37], 0, v5, s[34:35]
	s_add_i32 s38, s41, 1
	v_cmp_lt_u32_e64 s[38:39], s38, v254
	s_waitcnt lgkmcnt(6)
	v_cmp_eq_f32_e64 s[36:37], v3, v113
	v_cmp_lt_f32_e64 s[34:35], v3, v113
	s_and_b64 s[36:37], s[38:39], s[36:37]
	s_or_b64 s[34:35], s[34:35], s[36:37]
	v_addc_co_u32_e64 v5, s[36:37], 0, v5, s[34:35]
	s_add_i32 s38, s41, 2
	v_cmp_lt_u32_e64 s[38:39], s38, v254
	s_waitcnt lgkmcnt(5)
	v_cmp_eq_f32_e64 s[36:37], v3, v114
	v_cmp_lt_f32_e64 s[34:35], v3, v114
	s_and_b64 s[36:37], s[38:39], s[36:37]
	s_or_b64 s[34:35], s[34:35], s[36:37]
	v_addc_co_u32_e64 v5, s[36:37], 0, v5, s[34:35]
	s_add_i32 s38, s41, 3
	v_cmp_lt_u32_e64 s[38:39], s38, v254
	s_waitcnt lgkmcnt(4)
	v_cmp_eq_f32_e64 s[36:37], v3, v115
	v_cmp_lt_f32_e64 s[34:35], v3, v115
	s_and_b64 s[36:37], s[38:39], s[36:37]
	s_or_b64 s[34:35], s[34:35], s[36:37]
	v_addc_co_u32_e64 v5, s[36:37], 0, v5, s[34:35]
	s_add_i32 s38, s41, 4
	v_cmp_lt_u32_e64 s[38:39], s38, v254
	s_waitcnt lgkmcnt(3)
	v_cmp_eq_f32_e64 s[36:37], v3, v116
	v_cmp_lt_f32_e64 s[34:35], v3, v116
	s_and_b64 s[36:37], s[38:39], s[36:37]
	s_or_b64 s[34:35], s[34:35], s[36:37]
	v_addc_co_u32_e64 v5, s[36:37], 0, v5, s[34:35]
	s_add_i32 s38, s41, 5
	v_cmp_lt_u32_e64 s[38:39], s38, v254
	s_waitcnt lgkmcnt(2)
	v_cmp_eq_f32_e64 s[36:37], v3, v117
	v_cmp_lt_f32_e64 s[34:35], v3, v117
	s_and_b64 s[36:37], s[38:39], s[36:37]
	s_or_b64 s[34:35], s[34:35], s[36:37]
	v_addc_co_u32_e64 v5, s[36:37], 0, v5, s[34:35]
	s_add_i32 s38, s41, 6
	v_cmp_lt_u32_e64 s[38:39], s38, v254
	s_waitcnt lgkmcnt(1)
	v_cmp_eq_f32_e64 s[36:37], v3, v118
	v_cmp_lt_f32_e64 s[34:35], v3, v118
	s_and_b64 s[36:37], s[38:39], s[36:37]
	s_or_b64 s[34:35], s[34:35], s[36:37]
	v_addc_co_u32_e64 v5, s[36:37], 0, v5, s[34:35]
	s_add_i32 s38, s41, 7
	v_cmp_lt_u32_e64 s[38:39], s38, v254
	s_waitcnt lgkmcnt(0)
	v_cmp_eq_f32_e64 s[36:37], v3, v119
	v_cmp_lt_f32_e64 s[34:35], v3, v119
	s_and_b64 s[36:37], s[38:39], s[36:37]
	s_or_b64 s[34:35], s[34:35], s[36:37]
	v_addc_co_u32_e64 v5, s[36:37], 0, v5, s[34:35]
	s_add_i32 s41, s41, 8
	s_cmp_lg_u32 s41, 64
	s_cbranch_scc1 .LBB0_1890
.Lrk_exit_1:
	v_cmp_gt_u32_e64 s[34:35], 8, v5
	s_and_b64 vcc, vcc, s[34:35]
	v_cndmask_b32_e32 v1, 0, v2, vcc
	ds_bpermute_b32 v3, v76, v1
	s_waitcnt lgkmcnt(0)
	v_add_f32_e32 v1, v1, v3
	ds_bpermute_b32 v3, v77, v1
	s_waitcnt lgkmcnt(0)
	v_add_f32_e32 v1, v1, v3
	ds_bpermute_b32 v3, v78, v1
	s_waitcnt lgkmcnt(0)
	v_add_f32_e32 v1, v1, v3
	ds_bpermute_b32 v3, v79, v1
	s_waitcnt lgkmcnt(0)
	v_add_f32_e32 v1, v1, v3
	ds_bpermute_b32 v3, v80, v1
	s_waitcnt lgkmcnt(0)
	v_add_f32_e32 v3, v1, v3
	ds_bpermute_b32 v4, v81, v3
	s_and_saveexec_b64 s[34:35], vcc
	s_cbranch_execz .LBB0_1893
	s_add_i32 s36, s69, s87
	s_waitcnt lgkmcnt(0)
	v_add_f32_e32 v1, v3, v4
	v_lshl_or_b32 v6, s36, 3, v5
	v_div_scale_f32 v3, s[36:37], v1, v1, v2
	v_rcp_f32_e32 v10, v3
	v_ashrrev_i32_e32 v7, 31, v6
	v_lshlrev_b64 v[6:7], 2, v[6:7]
	v_lshl_add_u64 v[8:9], s[56:57], 0, v[6:7]
	ds_add_rtn_u32 v4, v85, v107
	global_store_dword v[8:9], v254, off
	v_fma_f32 v8, -v3, v10, 1.0
	v_fmac_f32_e32 v10, v8, v10
	v_div_scale_f32 v8, vcc, v2, v1, v2
	v_mul_f32_e32 v9, v8, v10
	v_fma_f32 v11, -v3, v9, v8
	v_fmac_f32_e32 v9, v11, v10
	v_fma_f32 v3, -v3, v9, v8
	v_div_fmas_f32 v3, v3, v10, v9
	v_div_fixup_f32 v1, v3, v1, v2
	v_mul_f32_e32 v1, 0x40200000, v1
	v_lshl_add_u64 v[2:3], s[58:59], 0, v[6:7]
	s_add_i32 s36, s40, s73
	global_store_dword v[2:3], v1, off
	s_waitcnt lgkmcnt(0)
	v_or_b32_e32 v1, v4, v86
	v_lshl_add_u32 v2, v5, 2, s36
	ds_write_b32 v2, v1

.Lrk_exit_2:
	v_cmp_gt_u32_e64 s[34:35], 8, v5
	s_and_b64 vcc, vcc, s[34:35]
	v_cndmask_b32_e32 v1, 0, v2, vcc
	ds_bpermute_b32 v3, v76, v1
	s_waitcnt lgkmcnt(0)
	v_add_f32_e32 v1, v1, v3
	ds_bpermute_b32 v3, v77, v1
	s_waitcnt lgkmcnt(0)
	v_add_f32_e32 v1, v1, v3
	ds_bpermute_b32 v3, v78, v1
	s_waitcnt lgkmcnt(0)
	v_add_f32_e32 v1, v1, v3
	ds_bpermute_b32 v3, v79, v1
	s_waitcnt lgkmcnt(0)
	v_add_f32_e32 v1, v1, v3
	ds_bpermute_b32 v3, v80, v1
	s_waitcnt lgkmcnt(0)
	v_add_f32_e32 v3, v1, v3
	ds_bpermute_b32 v4, v81, v3
	s_and_saveexec_b64 s[34:35], vcc
	s_cbranch_execz .LBB0_1897
	s_add_i32 s36, s74, s87
	s_waitcnt lgkmcnt(0)
	v_add_f32_e32 v1, v3, v4
	v_lshl_or_b32 v6, s36, 3, v5
	v_div_scale_f32 v3, s[36:37], v1, v1, v2
	v_rcp_f32_e32 v10, v3
	v_ashrrev_i32_e32 v7, 31, v6
	v_lshlrev_b64 v[6:7], 2, v[6:7]
	v_lshl_add_u64 v[8:9], s[56:57], 0, v[6:7]
	ds_add_rtn_u32 v4, v85, v107
	global_store_dword v[8:9], v254, off
	v_fma_f32 v8, -v3, v10, 1.0
	v_fmac_f32_e32 v10, v8, v10
	v_div_scale_f32 v8, vcc, v2, v1, v2
	v_mul_f32_e32 v9, v8, v10
	v_fma_f32 v11, -v3, v9, v8
	v_fmac_f32_e32 v9, v11, v10
	v_fma_f32 v3, -v3, v9, v8
	v_div_fmas_f32 v3, v3, v10, v9
	v_div_fixup_f32 v1, v3, v1, v2
	v_mul_f32_e32 v1, 0x40200000, v1
	v_lshl_add_u64 v[2:3], s[58:59], 0, v[6:7]
	s_add_i32 s36, s40, s77
	global_store_dword v[2:3], v1, off
	s_waitcnt lgkmcnt(0)
	v_or_b32_e32 v1, v4, v86
	v_lshl_add_u32 v2, v5, 2, s36
	ds_write_b32 v2, v1

.Lrk_exit_3:
	v_cmp_gt_u32_e64 s[34:35], 8, v5
	s_and_b64 vcc, vcc, s[34:35]
	v_cndmask_b32_e32 v1, 0, v2, vcc
	ds_bpermute_b32 v3, v76, v1
	s_waitcnt lgkmcnt(0)
	v_add_f32_e32 v1, v1, v3
	ds_bpermute_b32 v3, v77, v1
	s_waitcnt lgkmcnt(0)
	v_add_f32_e32 v1, v1, v3
	ds_bpermute_b32 v3, v78, v1
	s_waitcnt lgkmcnt(0)
	v_add_f32_e32 v1, v1, v3
	ds_bpermute_b32 v3, v79, v1
	s_waitcnt lgkmcnt(0)
	v_add_f32_e32 v1, v1, v3
	ds_bpermute_b32 v3, v80, v1
	s_waitcnt lgkmcnt(0)
	v_add_f32_e32 v3, v1, v3
	ds_bpermute_b32 v4, v81, v3
	s_and_saveexec_b64 s[34:35], vcc
	s_cbranch_execz .LBB0_1874
	s_add_i32 s36, s78, s87
	s_waitcnt lgkmcnt(0)
	v_add_f32_e32 v1, v3, v4
	v_lshl_or_b32 v6, s36, 3, v5
	v_div_scale_f32 v3, s[36:37], v1, v1, v2
	v_rcp_f32_e32 v10, v3
	v_ashrrev_i32_e32 v7, 31, v6
	v_lshlrev_b64 v[6:7], 2, v[6:7]
	v_lshl_add_u64 v[8:9], s[56:57], 0, v[6:7]
	ds_add_rtn_u32 v4, v85, v107
	global_store_dword v[8:9], v254, off
	v_fma_f32 v8, -v3, v10, 1.0
	v_fmac_f32_e32 v10, v8, v10
	v_div_scale_f32 v8, vcc, v2, v1, v2
	v_mul_f32_e32 v9, v8, v10
	v_fma_f32 v11, -v3, v9, v8
	v_fmac_f32_e32 v9, v11, v10
	v_fma_f32 v3, -v3, v9, v8
	v_div_fmas_f32 v3, v3, v10, v9
	v_div_fixup_f32 v1, v3, v1, v2
	v_mul_f32_e32 v1, 0x40200000, v1
	v_lshl_add_u64 v[2:3], s[58:59], 0, v[6:7]
	s_add_i32 s40, s40, s80
	global_store_dword v[2:3], v1, off
	s_waitcnt lgkmcnt(0)
	v_or_b32_e32 v1, v4, v86
	v_lshl_add_u32 v2, v5, 2, s40
	ds_write_b32 v2, v1
	s_branch .LBB0_1874
